# P2 tail LayerNorm-statistics row loop: next row's four 16-byte loads prefetched into spare VGPRs while the current row is reduced (two rows in flight per wave instead of one)
# baseline (speedup 1.0000x reference)
.LBB0_296:
	v_readlane_b32 s2, v255, 10
	s_add_i32 s8, s33, s2
	s_cmpk_gt_i32 s8, 0x1fff
	s_cbranch_scc1 .LBB0_301
	s_add_u32 s9, s0, 0x2b740000
	s_addc_u32 s10, s1, 0
	s_mul_i32 s3, s8, 0x6000
	s_mul_hi_i32 s2, s8, 0x6000
	s_add_u32 s0, s0, s3
	v_lshlrev_b32_e32 v2, 4, v74
	v_mov_b32_e32 v3, 0
	s_addc_u32 s1, s1, s2
	v_lshl_add_u64 v[4:5], s[0:1], 0, v[2:3]
	s_mov_b64 s[0:1], 0xf305c00
	s_lshl_b32 s2, s80, 4
	v_cmp_eq_u32_e32 vcc, 0, v74
	v_lshl_add_u64 v[4:5], v[4:5], 0, s[0:1]
	s_mul_hi_i32 s1, s78, 0x6000
	s_mul_i32 s0, s78, 0x6000
	s_add_i32 s2, s2, s61
	s_lshl_b32 s11, s81, 4
	v_mov_b32_e32 v1, 0x358637bd
	s_mov_b32 s12, 0x800000
	global_load_dwordx4 v[40:43], v[4:5], off offset:-3072
	global_load_dwordx4 v[44:47], v[4:5], off offset:-2048
	global_load_dwordx4 v[48:51], v[4:5], off offset:-1024
	global_load_dwordx4 v[52:55], v[4:5], off
	s_branch .LBB0_299

.LBB0_299:
	s_waitcnt vmcnt(0)
	v_mov_b64_e32 v[6:7], v[40:41]
	v_mov_b64_e32 v[8:9], v[42:43]
	v_mov_b64_e32 v[10:11], v[44:45]
	v_mov_b64_e32 v[12:13], v[46:47]
	v_mov_b64_e32 v[14:15], v[48:49]
	v_mov_b64_e32 v[16:17], v[50:51]
	v_mov_b64_e32 v[18:19], v[52:53]
	v_mov_b64_e32 v[20:21], v[54:55]
	s_add_i32 s15, s8, s78
	s_cmpk_gt_i32 s15, 0x1fff
	s_cbranch_scc1 .Lp2t_nopf
	v_lshl_add_u64 v[56:57], v[4:5], 0, s[0:1]
	global_load_dwordx4 v[40:43], v[56:57], off offset:-3072
	global_load_dwordx4 v[44:47], v[56:57], off offset:-2048
	global_load_dwordx4 v[48:51], v[56:57], off offset:-1024
	global_load_dwordx4 v[52:55], v[56:57], off
.Lp2t_nopf:
	v_lshlrev_b32_e32 v22, 16, v6
	v_and_b32_e32 v6, 0xffff0000, v6
	v_add_f32_e32 v2, 0, v22
	v_lshlrev_b32_e32 v23, 16, v7
	v_add_f32_e32 v2, v2, v6
	v_and_b32_e32 v7, 0xffff0000, v7
	v_add_f32_e32 v2, v2, v23
	v_lshlrev_b32_e32 v24, 16, v8
	v_add_f32_e32 v2, v2, v7
	v_and_b32_e32 v8, 0xffff0000, v8
	v_add_f32_e32 v2, v2, v24
	v_lshlrev_b32_e32 v25, 16, v9
	v_add_f32_e32 v2, v2, v8
	v_and_b32_e32 v9, 0xffff0000, v9
	v_add_f32_e32 v2, v2, v25
	v_lshlrev_b32_e32 v26, 16, v10
	v_add_f32_e32 v2, v2, v9
	v_and_b32_e32 v10, 0xffff0000, v10
	v_add_f32_e32 v2, v2, v26
	v_lshlrev_b32_e32 v27, 16, v11
	v_add_f32_e32 v2, v2, v10
	v_and_b32_e32 v11, 0xffff0000, v11
	v_add_f32_e32 v2, v2, v27
	v_lshlrev_b32_e32 v28, 16, v12
	v_add_f32_e32 v2, v2, v11
	v_and_b32_e32 v12, 0xffff0000, v12
	v_add_f32_e32 v2, v2, v28
	v_lshlrev_b32_e32 v29, 16, v13
	v_add_f32_e32 v2, v2, v12
	v_and_b32_e32 v13, 0xffff0000, v13
	v_add_f32_e32 v2, v2, v29
	v_lshlrev_b32_e32 v30, 16, v14
	v_add_f32_e32 v2, v2, v13
	v_and_b32_e32 v14, 0xffff0000, v14
	v_add_f32_e32 v2, v2, v30
	v_lshlrev_b32_e32 v31, 16, v15
	v_add_f32_e32 v2, v2, v14
	v_and_b32_e32 v15, 0xffff0000, v15
	v_add_f32_e32 v2, v2, v31
	v_lshlrev_b32_e32 v32, 16, v16
	v_add_f32_e32 v2, v2, v15
	v_and_b32_e32 v16, 0xffff0000, v16
	v_add_f32_e32 v2, v2, v32
	v_lshlrev_b32_e32 v33, 16, v17
	v_add_f32_e32 v2, v2, v16
	v_and_b32_e32 v17, 0xffff0000, v17
	v_add_f32_e32 v2, v2, v33
	v_lshlrev_b32_e32 v34, 16, v18
	v_add_f32_e32 v2, v2, v17
	v_and_b32_e32 v18, 0xffff0000, v18
	v_add_f32_e32 v2, v2, v34
	v_lshlrev_b32_e32 v35, 16, v19
	v_add_f32_e32 v2, v2, v18
	v_and_b32_e32 v19, 0xffff0000, v19
	v_add_f32_e32 v2, v2, v35
	v_lshlrev_b32_e32 v36, 16, v20
	v_add_f32_e32 v2, v2, v19
	v_and_b32_e32 v20, 0xffff0000, v20
	v_add_f32_e32 v2, v2, v36
	v_lshlrev_b32_e32 v37, 16, v21
	v_add_f32_e32 v2, v2, v20
	v_and_b32_e32 v21, 0xffff0000, v21
	v_add_f32_e32 v2, v2, v37
	v_add_f32_e32 v2, v2, v21
	s_nop 1
	v_add_f32_dpp v2, v2, v2 quad_perm:[1,0,3,2] row_mask:0xf bank_mask:0xf bound_ctrl:1
	s_nop 1
	v_add_f32_dpp v2, v2, v2 quad_perm:[2,3,0,1] row_mask:0xf bank_mask:0xf bound_ctrl:1
	s_nop 1
	v_add_f32_dpp v2, v2, v2 row_half_mirror row_mask:0xf bank_mask:0xf bound_ctrl:1
	s_nop 1
	v_add_f32_dpp v2, v2, v2 row_mirror row_mask:0xf bank_mask:0xf bound_ctrl:1
	s_nop 0
	v_readlane_b32 s4, v2, 16
	v_readlane_b32 s6, v2, 48
	v_readlane_b32 s3, v2, 0
	v_readlane_b32 s5, v2, 32
	v_mov_b32_e32 v2, s4
	v_mov_b32_e32 v38, s6
	v_add_f32_e32 v2, s3, v2
	v_add_f32_e32 v38, s5, v38
	v_add_f32_e32 v2, v2, v38
	v_fmac_f32_e32 v6, 0xba000000, v2
	v_fmac_f32_e32 v22, 0xba000000, v2
	v_mul_f32_e32 v6, v6, v6
	v_fmac_f32_e32 v23, 0xba000000, v2
	v_fmac_f32_e32 v6, v22, v22
	v_fmac_f32_e32 v7, 0xba000000, v2
	v_fmac_f32_e32 v6, v23, v23
	v_fmac_f32_e32 v24, 0xba000000, v2
	v_fmac_f32_e32 v6, v7, v7
	v_fmac_f32_e32 v8, 0xba000000, v2
	v_fmac_f32_e32 v6, v24, v24
	v_fmac_f32_e32 v25, 0xba000000, v2
	v_fmac_f32_e32 v6, v8, v8
	v_fmac_f32_e32 v9, 0xba000000, v2
	v_fmac_f32_e32 v6, v25, v25
	v_fmac_f32_e32 v26, 0xba000000, v2
	v_fmac_f32_e32 v6, v9, v9
	v_fmac_f32_e32 v10, 0xba000000, v2
	v_fmac_f32_e32 v6, v26, v26
	v_fmac_f32_e32 v27, 0xba000000, v2
	v_fmac_f32_e32 v6, v10, v10
	v_fmac_f32_e32 v11, 0xba000000, v2
	v_fmac_f32_e32 v6, v27, v27
	v_fmac_f32_e32 v28, 0xba000000, v2
	v_fmac_f32_e32 v6, v11, v11
	v_fmac_f32_e32 v12, 0xba000000, v2
	v_fmac_f32_e32 v6, v28, v28
	v_fmac_f32_e32 v29, 0xba000000, v2
	v_fmac_f32_e32 v6, v12, v12
	v_fmac_f32_e32 v13, 0xba000000, v2
	v_fmac_f32_e32 v6, v29, v29
	v_fmac_f32_e32 v30, 0xba000000, v2
	v_fmac_f32_e32 v6, v13, v13
	v_fmac_f32_e32 v14, 0xba000000, v2
	v_fmac_f32_e32 v6, v30, v30
	v_fmac_f32_e32 v31, 0xba000000, v2
	v_fmac_f32_e32 v6, v14, v14
	v_fmac_f32_e32 v15, 0xba000000, v2
	v_fmac_f32_e32 v6, v31, v31
	v_fmac_f32_e32 v32, 0xba000000, v2
	v_fmac_f32_e32 v6, v15, v15
	v_fmac_f32_e32 v16, 0xba000000, v2
	v_fmac_f32_e32 v6, v32, v32
	v_fmac_f32_e32 v33, 0xba000000, v2
	v_fmac_f32_e32 v6, v16, v16
	v_fmac_f32_e32 v17, 0xba000000, v2
	v_fmac_f32_e32 v6, v33, v33
	v_fmac_f32_e32 v34, 0xba000000, v2
	v_fmac_f32_e32 v6, v17, v17
	v_fmac_f32_e32 v18, 0xba000000, v2
	v_fmac_f32_e32 v6, v34, v34
	v_fmac_f32_e32 v35, 0xba000000, v2
	v_fmac_f32_e32 v6, v18, v18
	v_fmac_f32_e32 v19, 0xba000000, v2
	v_fmac_f32_e32 v6, v35, v35
	v_fmac_f32_e32 v36, 0xba000000, v2
	v_fmac_f32_e32 v6, v19, v19
	v_fmac_f32_e32 v20, 0xba000000, v2
	v_fmac_f32_e32 v6, v36, v36
	v_fmac_f32_e32 v37, 0xba000000, v2
	v_fmac_f32_e32 v6, v20, v20
	v_fmac_f32_e32 v21, 0xba000000, v2
	v_fmac_f32_e32 v6, v37, v37
	v_fmac_f32_e32 v6, v21, v21
	s_nop 1
	v_add_f32_dpp v6, v6, v6 quad_perm:[1,0,3,2] row_mask:0xf bank_mask:0xf bound_ctrl:1
	s_nop 1
	v_add_f32_dpp v6, v6, v6 quad_perm:[2,3,0,1] row_mask:0xf bank_mask:0xf bound_ctrl:1
	s_nop 1
	v_add_f32_dpp v6, v6, v6 row_half_mirror row_mask:0xf bank_mask:0xf bound_ctrl:1
	s_nop 1
	v_add_f32_dpp v6, v6, v6 row_mirror row_mask:0xf bank_mask:0xf bound_ctrl:1
	s_nop 0
	v_readlane_b32 s4, v6, 0
	v_readlane_b32 s13, v6, 16
	v_readlane_b32 s5, v6, 32
	v_readlane_b32 s14, v6, 48
	s_and_saveexec_b64 s[6:7], vcc
	s_cbranch_execz .LBB0_298
	v_mov_b32_e32 v8, s13
	v_mov_b32_e32 v9, s14
	v_pk_add_f32 v[8:9], s[4:5], v[8:9]
	v_mul_f32_e32 v6, 0x3a000000, v2
	v_add_f32_e32 v2, v8, v9
	v_fmamk_f32 v2, v2, 0x3a000000, v1
	v_mul_f32_e32 v7, 0x4b800000, v2
	v_cmp_gt_f32_e64 s[4:5], s12, v2
	s_ashr_i32 s3, s2, 31
	s_lshl_b64 s[14:15], s[2:3], 2
	v_cndmask_b32_e64 v2, v2, v7, s[4:5]
	v_rsq_f32_e32 v2, v2
	s_add_u32 s14, s9, s14
	s_addc_u32 s15, s10, s15
	v_mul_f32_e32 v7, 0x45800000, v2
	v_cndmask_b32_e64 v7, v2, v7, s[4:5]
	global_store_dwordx2 v3, v[6:7], s[14:15]
	s_branch .LBB0_298
